# out-projection epilogue (layers 1-3): the 16 residual-tile loads issued up front into spare VGPRs with one wait, instead of 16 dependent load-wait-store steps; on top of previous stack
# speedup vs baseline: 1.0064x; 1.0028x over previous
; __device__ __forceinline__ unsigned cvt_pk_bf16(float lo, float hi) { unsigned r; asm volatile("v_cvt_pk_bf16_f32 %0, %1, %2" : "=v"(r) : "v"(lo), "v"(hi)); return r; }
;     __device__ __forceinline__ void operator()(const f32x4 (&acc)[2][2][4][2], const Unit& u, int wr, int wc, int fr, int fq) const {
;         const int row0 = u.pm * BM + wr * 64 + fr, col0 = u.pn * BM + wc * 32 + 8 * fq;
;         const float* gp = gate + (size_t)((u.pm * BM) >> 12) * gstride + col0;
;         f32x4 gv[2][2];
; #pragma unroll
;         for (int bj = 0; bj < 2; ++bj)
; #pragma unroll
;             for (int n = 0; n < 2; ++n) gv[bj][n] = *(const f32x4*)(gp + bj * HALF + 4 * n) * accs;
; #pragma unroll
;         for (int ai = 0; ai < 2; ++ai)
; #pragma unroll
;             for (int m = 0; m < 4; ++m) { const size_t ro = (size_t)(row0 + ai * HALF + m * 16) * DM + col0;
; #pragma unroll
;                 for (int bj = 0; bj < 2; ++bj) {
;                     f32x4 b0, b1;
;                     if (x0) { b0 = *(const f32x4*)(x0 + ro + bj * HALF); b1 = *(const f32x4*)(x0 + ro + bj * HALF + 4); }
;                     else { const u32x4 w = *(const u32x4*)(xb + ro + bj * HALF); b0 = (f32x4){bf_lo(w.x), bf_hi(w.x), bf_lo(w.y), bf_hi(w.y)}; b1 = (f32x4){bf_lo(w.z), bf_hi(w.z), bf_lo(w.w), bf_hi(w.w)}; }
;                     const f32x4 v0 = b0 + gv[bj][0] * acc[ai][bj][m][0], v1 = b1 + gv[bj][1] * acc[ai][bj][m][1];
;                     u32x4 o; o.x = cvt_pk_bf16(v0[0], v0[1]); o.y = cvt_pk_bf16(v0[2], v0[3]); o.z = cvt_pk_bf16(v1[0], v1[1]); o.w = cvt_pk_bf16(v1[2], v1[3]);
;                     *(u32x4*)(xout + ro + bj * HALF) = o; } }
.LBB0_1916:
	v_mov_b32_e32 v140, v146
	s_lshl_b32 s25, s79, 8
	v_lshrrev_b32_e32 v128, 1, v140
	s_lshl_b32 s23, s38, 8
	v_and_or_b32 v128, v128, 24, s25
	s_ashr_i32 s25, s38, 4
	s_add_i32 s23, s23, s64
	s_mul_hi_i32 s38, s25, 0x6000
	s_mulk_i32 s25, 0x6000
	v_or_b32_e32 v136, s65, v128
	s_add_u32 s40, s62, s25
	v_and_or_b32 v142, v140, 15, s23
	s_addc_u32 s41, s63, s38
	v_ashrrev_i32_e32 v137, 31, v136
	v_ashrrev_i32_e32 v143, 31, v142
	v_lshl_add_u64 v[138:139], v[136:137], 2, s[40:41]
	v_lshlrev_b64 v[140:141], 11, v[142:143]
	global_load_dwordx4 v[128:131], v[138:139], off offset:16
	global_load_dwordx4 v[132:135], v[138:139], off
	v_lshl_add_u64 v[140:141], s[8:9], 0, v[140:141]
	v_lshlrev_b64 v[144:145], 1, v[136:137]
	v_lshl_add_u64 v[140:141], v[140:141], 0, v[144:145]
	v_mov_b32_e32 v236, 0x8000
	v_mov_b32_e32 v237, 0
	v_mov_b32_e32 v238, 0x40000
	v_mov_b32_e32 v239, 0
	global_load_dwordx4 v[172:175], v[140:141], off
	global_load_dwordx4 v[176:179], v[140:141], off offset:256
	v_lshl_add_u64 v[240:241], v[140:141], 0, v[236:237]
	global_load_dwordx4 v[180:183], v[240:241], off
	global_load_dwordx4 v[184:187], v[240:241], off offset:256
	v_lshl_add_u64 v[240:241], v[240:241], 0, v[236:237]
	global_load_dwordx4 v[188:191], v[240:241], off
	global_load_dwordx4 v[192:195], v[240:241], off offset:256
	v_lshl_add_u64 v[240:241], v[240:241], 0, v[236:237]
	global_load_dwordx4 v[196:199], v[240:241], off
	global_load_dwordx4 v[200:203], v[240:241], off offset:256
	v_lshl_add_u64 v[240:241], v[140:141], 0, v[238:239]
	global_load_dwordx4 v[204:207], v[240:241], off
	global_load_dwordx4 v[208:211], v[240:241], off offset:256
	v_lshl_add_u64 v[240:241], v[240:241], 0, v[236:237]
	global_load_dwordx4 v[212:215], v[240:241], off
	global_load_dwordx4 v[216:219], v[240:241], off offset:256
	v_lshl_add_u64 v[240:241], v[240:241], 0, v[236:237]
	global_load_dwordx4 v[220:223], v[240:241], off
	global_load_dwordx4 v[224:227], v[240:241], off offset:256
	v_lshl_add_u64 v[240:241], v[240:241], 0, v[236:237]
	global_load_dwordx4 v[228:231], v[240:241], off
	global_load_dwordx4 v[232:235], v[240:241], off offset:256
	global_load_dwordx4 v[162:165], v[138:139], off offset:528
	global_load_dwordx4 v[166:169], v[138:139], off offset:512
	s_waitcnt vmcnt(0)
	v_mov_b32_e32 v158, v172
	v_mov_b32_e32 v159, v173
	v_mov_b32_e32 v160, v174
	v_mov_b32_e32 v161, v175
	v_pk_mul_f32 v[138:139], v[134:135], s[12:13] op_sel_hi:[1,0]
	v_pk_mul_f32 v[136:137], v[132:133], s[12:13] op_sel_hi:[1,0]
	v_pk_mul_f32 v[134:135], v[130:131], s[12:13] op_sel_hi:[1,0]
	v_pk_mul_f32 v[132:133], v[128:129], s[12:13] op_sel_hi:[1,0]
	v_lshlrev_b32_e32 v128, 16, v158
	v_and_b32_e32 v129, 0xffff0000, v158
	v_lshlrev_b32_e32 v130, 16, v159
	v_and_b32_e32 v131, 0xffff0000, v159
	v_lshlrev_b32_e32 v158, 16, v160
	v_and_b32_e32 v159, 0xffff0000, v160
	v_lshlrev_b32_e32 v160, 16, v161
	v_and_b32_e32 v161, 0xffff0000, v161
	v_pk_fma_f32 v[126:127], v[126:127], v[138:139], v[130:131]
	v_pk_fma_f32 v[124:125], v[124:125], v[136:137], v[128:129]
	v_pk_fma_f32 v[122:123], v[122:123], v[134:135], v[160:161]
	v_pk_fma_f32 v[120:121], v[120:121], v[132:133], v[158:159]
	v_cvt_pk_bf16_f32 v128, v124, v125
	v_cvt_pk_bf16_f32 v129, v126, v127
	v_pk_mul_f32 v[124:125], v[164:165], s[12:13] op_sel_hi:[1,0]
	v_cvt_pk_bf16_f32 v130, v120, v121
	v_cvt_pk_bf16_f32 v131, v122, v123
	v_mov_b32_e32 v158, v176
	v_mov_b32_e32 v159, v177
	v_mov_b32_e32 v160, v178
	v_mov_b32_e32 v161, v179
	v_or_b32_e32 v120, 16, v142
	v_ashrrev_i32_e32 v121, 31, v120
	v_lshlrev_b64 v[120:121], 11, v[120:121]
	v_lshl_add_u64 v[120:121], s[8:9], 0, v[120:121]
	v_lshl_add_u64 v[170:171], v[120:121], 0, v[144:145]
	v_pk_mul_f32 v[120:121], v[168:169], s[12:13] op_sel_hi:[1,0]
	v_pk_mul_f32 v[122:123], v[166:167], s[12:13] op_sel_hi:[1,0]
	v_pk_mul_f32 v[126:127], v[162:163], s[12:13] op_sel_hi:[1,0]
	global_store_dwordx4 v[140:141], v[128:131], off
	s_nop 0
	s_nop 0
	v_lshlrev_b32_e32 v128, 16, v158
	v_and_b32_e32 v129, 0xffff0000, v158
	v_lshlrev_b32_e32 v130, 16, v159
	v_and_b32_e32 v131, 0xffff0000, v159
	v_lshlrev_b32_e32 v158, 16, v160
	v_and_b32_e32 v159, 0xffff0000, v160
	v_lshlrev_b32_e32 v160, 16, v161
	v_and_b32_e32 v161, 0xffff0000, v161
	v_pk_fma_f32 v[114:115], v[114:115], v[120:121], v[130:131]
	v_pk_fma_f32 v[112:113], v[112:113], v[122:123], v[128:129]
	v_pk_fma_f32 v[128:129], v[110:111], v[124:125], v[160:161]
	v_pk_fma_f32 v[110:111], v[108:109], v[126:127], v[158:159]
	v_cvt_pk_bf16_f32 v108, v112, v113
	v_cvt_pk_bf16_f32 v109, v114, v115
	s_nop 0
	v_cvt_pk_bf16_f32 v110, v110, v111
	v_cvt_pk_bf16_f32 v111, v128, v129
	v_mov_b32_e32 v112, v180
	v_mov_b32_e32 v113, v181
	v_mov_b32_e32 v114, v182
	v_mov_b32_e32 v115, v183
	s_nop 0
	global_store_dwordx4 v[140:141], v[108:111], off offset:256
	s_nop 0
	s_nop 0
	v_lshlrev_b32_e32 v108, 16, v112
	v_and_b32_e32 v109, 0xffff0000, v112
	v_lshlrev_b32_e32 v110, 16, v113
	v_and_b32_e32 v111, 0xffff0000, v113
	v_lshlrev_b32_e32 v112, 16, v114
	v_and_b32_e32 v113, 0xffff0000, v114
	v_lshlrev_b32_e32 v114, 16, v115
	v_and_b32_e32 v115, 0xffff0000, v115
	v_pk_fma_f32 v[110:111], v[118:119], v[138:139], v[110:111]
	v_pk_fma_f32 v[108:109], v[116:117], v[136:137], v[108:109]
	v_pk_fma_f32 v[114:115], v[106:107], v[134:135], v[114:115]
	v_pk_fma_f32 v[106:107], v[104:105], v[132:133], v[112:113]
	v_cvt_pk_bf16_f32 v104, v108, v109
	v_cvt_pk_bf16_f32 v105, v110, v111
	v_or_b32_e32 v112, 32, v142
	v_cvt_pk_bf16_f32 v106, v106, v107
	v_cvt_pk_bf16_f32 v107, v114, v115
	v_mov_b32_e32 v108, v184
	v_mov_b32_e32 v109, v185
	v_mov_b32_e32 v110, v186
	v_mov_b32_e32 v111, v187
; __device__ __forceinline__ unsigned cvt_pk_bf16(float lo, float hi) { unsigned r; asm volatile("v_cvt_pk_bf16_f32 %0, %1, %2" : "=v"(r) : "v"(lo), "v"(hi)); return r; }
;     __device__ __forceinline__ void operator()(const f32x4 (&acc)[2][2][4][2], const Unit& u, int wr, int wc, int fr, int fq) const {
;     ...
;         for (int ai = 0; ai < 2; ++ai)
; #pragma unroll
;             for (int m = 0; m < 4; ++m) { const size_t ro = (size_t)(row0 + ai * HALF + m * 16) * DM + col0;
; #pragma unroll
;                 for (int bj = 0; bj < 2; ++bj) {
;                     f32x4 b0, b1;
;                     if (x0) { b0 = *(const f32x4*)(x0 + ro + bj * HALF); b1 = *(const f32x4*)(x0 + ro + bj * HALF + 4); }
;                     else { const u32x4 w = *(const u32x4*)(xb + ro + bj * HALF); b0 = (f32x4){bf_lo(w.x), bf_hi(w.x), bf_lo(w.y), bf_hi(w.y)}; b1 = (f32x4){bf_lo(w.z), bf_hi(w.z), bf_lo(w.w), bf_hi(w.w)}; }
;                     const f32x4 v0 = b0 + gv[bj][0] * acc[ai][bj][m][0], v1 = b1 + gv[bj][1] * acc[ai][bj][m][1];
;                     u32x4 o; o.x = cvt_pk_bf16(v0[0], v0[1]); o.y = cvt_pk_bf16(v0[2], v0[3]); o.z = cvt_pk_bf16(v1[0], v1[1]); o.w = cvt_pk_bf16(v1[2], v1[3]);
;                     *(u32x4*)(xout + ro + bj * HALF) = o; } }
	v_ashrrev_i32_e32 v113, 31, v112
	v_lshlrev_b64 v[112:113], 11, v[112:113]
	v_lshl_add_u64 v[112:113], s[8:9], 0, v[112:113]
	global_store_dwordx4 v[170:171], v[104:107], off
	s_nop 0
	v_lshl_add_u64 v[112:113], v[112:113], 0, v[144:145]
	v_lshlrev_b32_e32 v104, 16, v108
	v_and_b32_e32 v105, 0xffff0000, v108
	v_lshlrev_b32_e32 v106, 16, v109
	v_and_b32_e32 v107, 0xffff0000, v109
	v_lshlrev_b32_e32 v108, 16, v110
	v_and_b32_e32 v109, 0xffff0000, v110
	v_lshlrev_b32_e32 v110, 16, v111
	v_and_b32_e32 v111, 0xffff0000, v111
	v_pk_fma_f32 v[98:99], v[98:99], v[120:121], v[106:107]
	v_pk_fma_f32 v[96:97], v[96:97], v[122:123], v[104:105]
	v_pk_fma_f32 v[104:105], v[94:95], v[124:125], v[110:111]
	v_pk_fma_f32 v[94:95], v[92:93], v[126:127], v[108:109]
	v_cvt_pk_bf16_f32 v92, v96, v97
	v_cvt_pk_bf16_f32 v93, v98, v99
	s_nop 0
	v_cvt_pk_bf16_f32 v94, v94, v95
	v_cvt_pk_bf16_f32 v95, v104, v105
	v_mov_b32_e32 v96, v188
	v_mov_b32_e32 v97, v189
	v_mov_b32_e32 v98, v190
	v_mov_b32_e32 v99, v191
	s_nop 0
	global_store_dwordx4 v[170:171], v[92:95], off offset:256
	s_nop 0
	s_nop 0
	v_lshlrev_b32_e32 v92, 16, v96
	v_and_b32_e32 v93, 0xffff0000, v96
	v_lshlrev_b32_e32 v94, 16, v97
	v_and_b32_e32 v95, 0xffff0000, v97
	v_lshlrev_b32_e32 v96, 16, v98
	v_and_b32_e32 v97, 0xffff0000, v98
	v_lshlrev_b32_e32 v98, 16, v99
	v_and_b32_e32 v99, 0xffff0000, v99
	v_pk_fma_f32 v[94:95], v[102:103], v[138:139], v[94:95]
	v_pk_fma_f32 v[92:93], v[100:101], v[136:137], v[92:93]
	v_pk_fma_f32 v[98:99], v[90:91], v[134:135], v[98:99]
	v_pk_fma_f32 v[90:91], v[88:89], v[132:133], v[96:97]
	v_cvt_pk_bf16_f32 v88, v92, v93
	v_cvt_pk_bf16_f32 v89, v94, v95
	v_or_b32_e32 v96, 48, v142
	v_cvt_pk_bf16_f32 v90, v90, v91
	v_cvt_pk_bf16_f32 v91, v98, v99
	v_mov_b32_e32 v92, v192
	v_mov_b32_e32 v93, v193
	v_mov_b32_e32 v94, v194
	v_mov_b32_e32 v95, v195
	v_ashrrev_i32_e32 v97, 31, v96
	v_lshlrev_b64 v[96:97], 11, v[96:97]
	v_lshl_add_u64 v[96:97], s[8:9], 0, v[96:97]
	global_store_dwordx4 v[112:113], v[88:91], off
	s_nop 0
	v_lshl_add_u64 v[96:97], v[96:97], 0, v[144:145]
	v_lshlrev_b32_e32 v88, 16, v92
	v_and_b32_e32 v89, 0xffff0000, v92
	v_lshlrev_b32_e32 v90, 16, v93
	v_and_b32_e32 v91, 0xffff0000, v93
	v_lshlrev_b32_e32 v92, 16, v94
	v_and_b32_e32 v93, 0xffff0000, v94
	v_lshlrev_b32_e32 v94, 16, v95
	v_and_b32_e32 v95, 0xffff0000, v95
	v_pk_fma_f32 v[82:83], v[82:83], v[120:121], v[90:91]
	v_pk_fma_f32 v[80:81], v[80:81], v[122:123], v[88:89]
	v_pk_fma_f32 v[88:89], v[78:79], v[124:125], v[94:95]
	v_pk_fma_f32 v[78:79], v[76:77], v[126:127], v[92:93]
	v_cvt_pk_bf16_f32 v76, v80, v81
	v_cvt_pk_bf16_f32 v77, v82, v83
	s_nop 0
	v_cvt_pk_bf16_f32 v78, v78, v79
	v_cvt_pk_bf16_f32 v79, v88, v89
	v_mov_b32_e32 v80, v196
	v_mov_b32_e32 v81, v197
	v_mov_b32_e32 v82, v198
	v_mov_b32_e32 v83, v199
	s_nop 0
	global_store_dwordx4 v[112:113], v[76:79], off offset:256
	s_nop 0
	s_nop 0
	v_lshlrev_b32_e32 v76, 16, v80
	v_and_b32_e32 v77, 0xffff0000, v80
	v_lshlrev_b32_e32 v78, 16, v81
	v_and_b32_e32 v79, 0xffff0000, v81
	v_lshlrev_b32_e32 v80, 16, v82
	v_and_b32_e32 v81, 0xffff0000, v82
	v_lshlrev_b32_e32 v82, 16, v83
	v_and_b32_e32 v83, 0xffff0000, v83
	v_pk_fma_f32 v[78:79], v[86:87], v[138:139], v[78:79]
	v_pk_fma_f32 v[76:77], v[84:85], v[136:137], v[76:77]
	v_pk_fma_f32 v[82:83], v[74:75], v[134:135], v[82:83]
	v_pk_fma_f32 v[74:75], v[72:73], v[132:133], v[80:81]
	v_cvt_pk_bf16_f32 v72, v76, v77
	v_cvt_pk_bf16_f32 v73, v78, v79
	v_add_co_u32_e32 v80, vcc, s75, v140
	v_cvt_pk_bf16_f32 v74, v74, v75
	v_cvt_pk_bf16_f32 v75, v82, v83
	v_mov_b32_e32 v76, v200
	v_mov_b32_e32 v77, v201
	v_mov_b32_e32 v78, v202
	v_mov_b32_e32 v79, v203
	s_nop 0
	v_addc_co_u32_e32 v81, vcc, 0, v141, vcc
	global_store_dwordx4 v[96:97], v[72:75], off
	s_nop 0
	s_nop 0
	v_lshlrev_b32_e32 v72, 16, v76
	v_and_b32_e32 v73, 0xffff0000, v76
	v_lshlrev_b32_e32 v74, 16, v77
	v_and_b32_e32 v75, 0xffff0000, v77
	v_lshlrev_b32_e32 v76, 16, v78
	v_and_b32_e32 v77, 0xffff0000, v78
	v_lshlrev_b32_e32 v78, 16, v79
	v_and_b32_e32 v79, 0xffff0000, v79
	v_pk_fma_f32 v[70:71], v[70:71], v[120:121], v[74:75]
	v_pk_fma_f32 v[68:69], v[68:69], v[122:123], v[72:73]
	v_pk_fma_f32 v[72:73], v[66:67], v[124:125], v[78:79]
	v_pk_fma_f32 v[66:67], v[64:65], v[126:127], v[76:77]
	v_cvt_pk_bf16_f32 v64, v68, v69
	v_cvt_pk_bf16_f32 v65, v70, v71
	s_nop 0
	v_cvt_pk_bf16_f32 v66, v66, v67
	v_cvt_pk_bf16_f32 v67, v72, v73
	v_mov_b32_e32 v68, v204
	v_mov_b32_e32 v69, v205
	v_mov_b32_e32 v70, v206
	v_mov_b32_e32 v71, v207
	v_lshl_add_u64 v[72:73], v[140:141], 0, s[4:5]
	global_store_dwordx4 v[96:97], v[64:67], off offset:256
	s_nop 0
	s_nop 0
	v_lshlrev_b32_e32 v64, 16, v68
	v_and_b32_e32 v65, 0xffff0000, v68
	v_lshlrev_b32_e32 v66, 16, v69
	v_and_b32_e32 v67, 0xffff0000, v69
	v_lshlrev_b32_e32 v68, 16, v70
	v_and_b32_e32 v69, 0xffff0000, v70
	v_lshlrev_b32_e32 v70, 16, v71
	v_and_b32_e32 v71, 0xffff0000, v71
	v_pk_fma_f32 v[62:63], v[62:63], v[138:139], v[66:67]
	v_pk_fma_f32 v[60:61], v[60:61], v[136:137], v[64:65]
	v_pk_fma_f32 v[64:65], v[58:59], v[134:135], v[70:71]
	v_pk_fma_f32 v[58:59], v[56:57], v[132:133], v[68:69]
	v_cvt_pk_bf16_f32 v56, v60, v61
	v_cvt_pk_bf16_f32 v57, v62, v63
	s_nop 0
	v_cvt_pk_bf16_f32 v58, v58, v59
	v_cvt_pk_bf16_f32 v59, v64, v65
	v_mov_b32_e32 v60, v208
	v_mov_b32_e32 v61, v209
	v_mov_b32_e32 v62, v210
	v_mov_b32_e32 v63, v211
	v_add_co_u32_e32 v64, vcc, s76, v140
	global_store_dwordx4 v[80:81], v[56:59], off
	s_nop 0
	v_addc_co_u32_e32 v65, vcc, 0, v141, vcc
	v_lshlrev_b32_e32 v56, 16, v60
	v_and_b32_e32 v57, 0xffff0000, v60
	v_lshlrev_b32_e32 v58, 16, v61
	v_and_b32_e32 v59, 0xffff0000, v61
	v_lshlrev_b32_e32 v60, 16, v62
; __device__ __forceinline__ unsigned cvt_pk_bf16(float lo, float hi) { unsigned r; asm volatile("v_cvt_pk_bf16_f32 %0, %1, %2" : "=v"(r) : "v"(lo), "v"(hi)); return r; }
;     __device__ __forceinline__ void operator()(const f32x4 (&acc)[2][2][4][2], const Unit& u, int wr, int wc, int fr, int fq) const {
;     ...
;         for (int ai = 0; ai < 2; ++ai)
; #pragma unroll
;             for (int m = 0; m < 4; ++m) { const size_t ro = (size_t)(row0 + ai * HALF + m * 16) * DM + col0;
; #pragma unroll
;                 for (int bj = 0; bj < 2; ++bj) {
;                     f32x4 b0, b1;
;                     if (x0) { b0 = *(const f32x4*)(x0 + ro + bj * HALF); b1 = *(const f32x4*)(x0 + ro + bj * HALF + 4); }
;                     else { const u32x4 w = *(const u32x4*)(xb + ro + bj * HALF); b0 = (f32x4){bf_lo(w.x), bf_hi(w.x), bf_lo(w.y), bf_hi(w.y)}; b1 = (f32x4){bf_lo(w.z), bf_hi(w.z), bf_lo(w.w), bf_hi(w.w)}; }
;                     const f32x4 v0 = b0 + gv[bj][0] * acc[ai][bj][m][0], v1 = b1 + gv[bj][1] * acc[ai][bj][m][1];
;                     u32x4 o; o.x = cvt_pk_bf16(v0[0], v0[1]); o.y = cvt_pk_bf16(v0[2], v0[3]); o.z = cvt_pk_bf16(v1[0], v1[1]); o.w = cvt_pk_bf16(v1[2], v1[3]);
;                     *(u32x4*)(xout + ro + bj * HALF) = o; } }
	v_and_b32_e32 v61, 0xffff0000, v62
	v_lshlrev_b32_e32 v62, 16, v63
	v_and_b32_e32 v63, 0xffff0000, v63
	v_pk_fma_f32 v[54:55], v[54:55], v[120:121], v[58:59]
	v_pk_fma_f32 v[52:53], v[52:53], v[122:123], v[56:57]
	v_pk_fma_f32 v[56:57], v[46:47], v[124:125], v[62:63]
	v_pk_fma_f32 v[46:47], v[44:45], v[126:127], v[60:61]
	v_cvt_pk_bf16_f32 v44, v52, v53
	v_cvt_pk_bf16_f32 v45, v54, v55
	s_nop 0
	v_cvt_pk_bf16_f32 v46, v46, v47
	v_cvt_pk_bf16_f32 v47, v56, v57
	v_mov_b32_e32 v52, v212
	v_mov_b32_e32 v53, v213
	v_mov_b32_e32 v54, v214
	v_mov_b32_e32 v55, v215
	v_lshl_add_u64 v[56:57], v[140:141], 0, s[14:15]
	global_store_dwordx4 v[72:73], v[44:47], off offset:256
	s_nop 0
	s_nop 0
	v_lshlrev_b32_e32 v44, 16, v52
	v_and_b32_e32 v45, 0xffff0000, v52
	v_lshlrev_b32_e32 v46, 16, v53
	v_and_b32_e32 v47, 0xffff0000, v53
	v_lshlrev_b32_e32 v52, 16, v54
	v_and_b32_e32 v53, 0xffff0000, v54
	v_lshlrev_b32_e32 v54, 16, v55
	v_and_b32_e32 v55, 0xffff0000, v55
	v_pk_fma_f32 v[46:47], v[50:51], v[138:139], v[46:47]
	v_pk_fma_f32 v[44:45], v[48:49], v[136:137], v[44:45]
	v_pk_fma_f32 v[48:49], v[42:43], v[134:135], v[54:55]
	v_pk_fma_f32 v[42:43], v[40:41], v[132:133], v[52:53]
	v_cvt_pk_bf16_f32 v40, v44, v45
	v_cvt_pk_bf16_f32 v41, v46, v47
	s_nop 0
	v_cvt_pk_bf16_f32 v42, v42, v43
	v_cvt_pk_bf16_f32 v43, v48, v49
	v_mov_b32_e32 v44, v216
	v_mov_b32_e32 v45, v217
	v_mov_b32_e32 v46, v218
	v_mov_b32_e32 v47, v219
	v_add_co_u32_e32 v48, vcc, s77, v140
	global_store_dwordx4 v[64:65], v[40:43], off
	s_nop 0
	v_addc_co_u32_e32 v49, vcc, 0, v141, vcc
	v_lshlrev_b32_e32 v40, 16, v44
	v_and_b32_e32 v41, 0xffff0000, v44
	v_lshlrev_b32_e32 v42, 16, v45
	v_and_b32_e32 v43, 0xffff0000, v45
	v_lshlrev_b32_e32 v44, 16, v46
	v_and_b32_e32 v45, 0xffff0000, v46
	v_lshlrev_b32_e32 v46, 16, v47
	v_and_b32_e32 v47, 0xffff0000, v47
	v_pk_fma_f32 v[38:39], v[38:39], v[120:121], v[42:43]
	v_pk_fma_f32 v[36:37], v[36:37], v[122:123], v[40:41]
	v_pk_fma_f32 v[40:41], v[30:31], v[124:125], v[46:47]
	v_pk_fma_f32 v[30:31], v[28:29], v[126:127], v[44:45]
	v_cvt_pk_bf16_f32 v28, v36, v37
	v_cvt_pk_bf16_f32 v29, v38, v39
	s_nop 0
	v_cvt_pk_bf16_f32 v30, v30, v31
	v_cvt_pk_bf16_f32 v31, v40, v41
	v_mov_b32_e32 v36, v220
	v_mov_b32_e32 v37, v221
	v_mov_b32_e32 v38, v222
	v_mov_b32_e32 v39, v223
	v_lshl_add_u64 v[40:41], v[140:141], 0, s[16:17]
	global_store_dwordx4 v[56:57], v[28:31], off offset:256
	s_nop 0
	s_nop 0
	v_lshlrev_b32_e32 v28, 16, v36
	v_and_b32_e32 v29, 0xffff0000, v36
	v_lshlrev_b32_e32 v30, 16, v37
	v_and_b32_e32 v31, 0xffff0000, v37
	v_lshlrev_b32_e32 v36, 16, v38
	v_and_b32_e32 v37, 0xffff0000, v38
	v_lshlrev_b32_e32 v38, 16, v39
	v_and_b32_e32 v39, 0xffff0000, v39
	v_pk_fma_f32 v[30:31], v[34:35], v[138:139], v[30:31]
	v_pk_fma_f32 v[28:29], v[32:33], v[136:137], v[28:29]
	v_pk_fma_f32 v[32:33], v[26:27], v[134:135], v[38:39]
	v_pk_fma_f32 v[26:27], v[24:25], v[132:133], v[36:37]
	v_cvt_pk_bf16_f32 v24, v28, v29
	v_cvt_pk_bf16_f32 v25, v30, v31
	s_nop 0
	v_cvt_pk_bf16_f32 v26, v26, v27
	v_cvt_pk_bf16_f32 v27, v32, v33
	v_mov_b32_e32 v28, v224
	v_mov_b32_e32 v29, v225
	v_mov_b32_e32 v30, v226
	v_mov_b32_e32 v31, v227
	v_add_co_u32_e32 v32, vcc, s78, v140
	global_store_dwordx4 v[48:49], v[24:27], off
	s_nop 0
	v_addc_co_u32_e32 v33, vcc, 0, v141, vcc
	s_andn2_b64 vcc, exec, s[2:3]
	s_mov_b64 s[2:3], -1
	v_lshlrev_b32_e32 v24, 16, v28
	v_and_b32_e32 v25, 0xffff0000, v28
	v_lshlrev_b32_e32 v26, 16, v29
	v_and_b32_e32 v27, 0xffff0000, v29
	v_lshlrev_b32_e32 v28, 16, v30
	v_and_b32_e32 v29, 0xffff0000, v30
	v_lshlrev_b32_e32 v30, 16, v31
	v_and_b32_e32 v31, 0xffff0000, v31
	v_pk_fma_f32 v[22:23], v[22:23], v[120:121], v[26:27]
	v_pk_fma_f32 v[20:21], v[20:21], v[122:123], v[24:25]
	v_pk_fma_f32 v[24:25], v[14:15], v[124:125], v[30:31]
	v_pk_fma_f32 v[14:15], v[12:13], v[126:127], v[28:29]
	v_cvt_pk_bf16_f32 v12, v20, v21
	v_cvt_pk_bf16_f32 v13, v22, v23
	s_nop 0
	v_cvt_pk_bf16_f32 v14, v14, v15
	v_cvt_pk_bf16_f32 v15, v24, v25
	v_mov_b32_e32 v20, v228
	v_mov_b32_e32 v21, v229
	v_mov_b32_e32 v22, v230
	v_mov_b32_e32 v23, v231
	v_lshl_add_u64 v[24:25], v[140:141], 0, s[20:21]
	global_store_dwordx4 v[40:41], v[12:15], off offset:256
	s_nop 0
	s_nop 0
	v_lshlrev_b32_e32 v12, 16, v20
	v_and_b32_e32 v13, 0xffff0000, v20
	v_lshlrev_b32_e32 v14, 16, v21
	v_and_b32_e32 v15, 0xffff0000, v21
	v_lshlrev_b32_e32 v20, 16, v22
	v_and_b32_e32 v21, 0xffff0000, v22
	v_lshlrev_b32_e32 v22, 16, v23
	v_and_b32_e32 v23, 0xffff0000, v23
	v_pk_fma_f32 v[14:15], v[18:19], v[138:139], v[14:15]
	v_pk_fma_f32 v[12:13], v[16:17], v[136:137], v[12:13]
	v_pk_fma_f32 v[16:17], v[10:11], v[134:135], v[22:23]
	v_pk_fma_f32 v[10:11], v[8:9], v[132:133], v[20:21]
	v_cvt_pk_bf16_f32 v8, v12, v13
	v_cvt_pk_bf16_f32 v9, v14, v15
	s_nop 0
	v_cvt_pk_bf16_f32 v10, v10, v11
	v_cvt_pk_bf16_f32 v11, v16, v17
	v_mov_b32_e32 v12, v232
	v_mov_b32_e32 v13, v233
	v_mov_b32_e32 v14, v234
	v_mov_b32_e32 v15, v235
	s_nop 0
	global_store_dwordx4 v[32:33], v[8:11], off
	s_nop 0
	s_nop 0
	v_lshlrev_b32_e32 v8, 16, v12
	v_and_b32_e32 v9, 0xffff0000, v12
	v_lshlrev_b32_e32 v10, 16, v13
	v_and_b32_e32 v11, 0xffff0000, v13
	v_lshlrev_b32_e32 v12, 16, v14
	v_and_b32_e32 v13, 0xffff0000, v14
	v_lshlrev_b32_e32 v14, 16, v15
	v_and_b32_e32 v15, 0xffff0000, v15
	v_pk_fma_f32 v[4:5], v[4:5], v[122:123], v[8:9]
	v_pk_fma_f32 v[8:9], v[2:3], v[124:125], v[14:15]
	v_pk_fma_f32 v[2:3], v[0:1], v[126:127], v[12:13]
	v_pk_fma_f32 v[6:7], v[6:7], v[120:121], v[10:11]
	v_cvt_pk_bf16_f32 v0, v4, v5
	s_nop 0
	v_cvt_pk_bf16_f32 v1, v6, v7
	v_cvt_pk_bf16_f32 v2, v2, v3
	v_cvt_pk_bf16_f32 v3, v8, v9
	global_store_dwordx4 v[24:25], v[0:3], off offset:256
	s_cbranch_vccnz .LBB0_1905
	s_andn2_b64 vcc, exec, s[6:7]
	s_cbranch_vccnz .LBB0_1904
	s_barrier
	s_branch .LBB0_1904

; __device__ __forceinline__ unsigned cvt_pk_bf16(float lo, float hi) { unsigned r; asm volatile("v_cvt_pk_bf16_f32 %0, %1, %2" : "=v"(r) : "v"(lo), "v"(hi)); return r; }
;     __device__ __forceinline__ void operator()(const f32x4 (&acc)[2][2][4][2], const Unit& u, int wr, int wc, int fr, int fq) const {
;         const int row0 = u.pm * BM + wr * 64 + fr, col0 = u.pn * BM + wc * 32 + 8 * fq;
;         const float* gp = gate + (size_t)((u.pm * BM) >> 12) * gstride + col0;
;         f32x4 gv[2][2];
; #pragma unroll
;         for (int bj = 0; bj < 2; ++bj)
; #pragma unroll
;             for (int n = 0; n < 2; ++n) gv[bj][n] = *(const f32x4*)(gp + bj * HALF + 4 * n) * accs;
; #pragma unroll
;         for (int ai = 0; ai < 2; ++ai)
; #pragma unroll
;             for (int m = 0; m < 4; ++m) { const size_t ro = (size_t)(row0 + ai * HALF + m * 16) * DM + col0;
; #pragma unroll
;                 for (int bj = 0; bj < 2; ++bj) {
;                     f32x4 b0, b1;
;                     if (x0) { b0 = *(const f32x4*)(x0 + ro + bj * HALF); b1 = *(const f32x4*)(x0 + ro + bj * HALF + 4); }
;                     else { const u32x4 w = *(const u32x4*)(xb + ro + bj * HALF); b0 = (f32x4){bf_lo(w.x), bf_hi(w.x), bf_lo(w.y), bf_hi(w.y)}; b1 = (f32x4){bf_lo(w.z), bf_hi(w.z), bf_lo(w.w), bf_hi(w.w)}; }
;                     const f32x4 v0 = b0 + gv[bj][0] * acc[ai][bj][m][0], v1 = b1 + gv[bj][1] * acc[ai][bj][m][1];
;                     u32x4 o; o.x = cvt_pk_bf16(v0[0], v0[1]); o.y = cvt_pk_bf16(v0[2], v0[3]); o.z = cvt_pk_bf16(v1[0], v1[1]); o.w = cvt_pk_bf16(v1[2], v1[3]);
;                     *(u32x4*)(xout + ro + bj * HALF) = o; } }
.LBB0_3287:
	v_mov_b32_e32 v140, v146
	s_lshl_b32 s25, s79, 8
	v_lshrrev_b32_e32 v128, 1, v140
	s_lshl_b32 s23, s38, 8
	v_and_or_b32 v128, v128, 24, s25
	s_ashr_i32 s25, s38, 4
	s_add_i32 s23, s23, s64
	s_mul_hi_i32 s38, s25, 0x6000
	s_mulk_i32 s25, 0x6000
	v_or_b32_e32 v136, s65, v128
	s_add_u32 s40, s62, s25
	v_and_or_b32 v142, v140, 15, s23
	s_addc_u32 s41, s63, s38
	v_ashrrev_i32_e32 v137, 31, v136
	v_ashrrev_i32_e32 v143, 31, v142
	v_lshl_add_u64 v[138:139], v[136:137], 2, s[40:41]
	v_lshlrev_b64 v[140:141], 11, v[142:143]
	global_load_dwordx4 v[128:131], v[138:139], off offset:16
	global_load_dwordx4 v[132:135], v[138:139], off
	v_lshl_add_u64 v[140:141], s[6:7], 0, v[140:141]
	v_lshlrev_b64 v[144:145], 1, v[136:137]
	v_lshl_add_u64 v[140:141], v[140:141], 0, v[144:145]
	v_mov_b32_e32 v236, 0x8000
	v_mov_b32_e32 v237, 0
	v_mov_b32_e32 v238, 0x40000
	v_mov_b32_e32 v239, 0
	global_load_dwordx4 v[172:175], v[140:141], off
	global_load_dwordx4 v[176:179], v[140:141], off offset:256
	v_lshl_add_u64 v[240:241], v[140:141], 0, v[236:237]
	global_load_dwordx4 v[180:183], v[240:241], off
	global_load_dwordx4 v[184:187], v[240:241], off offset:256
	v_lshl_add_u64 v[240:241], v[240:241], 0, v[236:237]
	global_load_dwordx4 v[188:191], v[240:241], off
	global_load_dwordx4 v[192:195], v[240:241], off offset:256
	v_lshl_add_u64 v[240:241], v[240:241], 0, v[236:237]
	global_load_dwordx4 v[196:199], v[240:241], off
	global_load_dwordx4 v[200:203], v[240:241], off offset:256
	v_lshl_add_u64 v[240:241], v[140:141], 0, v[238:239]
	global_load_dwordx4 v[204:207], v[240:241], off
	global_load_dwordx4 v[208:211], v[240:241], off offset:256
	v_lshl_add_u64 v[240:241], v[240:241], 0, v[236:237]
	global_load_dwordx4 v[212:215], v[240:241], off
	global_load_dwordx4 v[216:219], v[240:241], off offset:256
	v_lshl_add_u64 v[240:241], v[240:241], 0, v[236:237]
	global_load_dwordx4 v[220:223], v[240:241], off
	global_load_dwordx4 v[224:227], v[240:241], off offset:256
	v_lshl_add_u64 v[240:241], v[240:241], 0, v[236:237]
	global_load_dwordx4 v[228:231], v[240:241], off
	global_load_dwordx4 v[232:235], v[240:241], off offset:256
	global_load_dwordx4 v[162:165], v[138:139], off offset:528
	global_load_dwordx4 v[166:169], v[138:139], off offset:512
	s_waitcnt vmcnt(0)
	v_mov_b32_e32 v158, v172
	v_mov_b32_e32 v159, v173
	v_mov_b32_e32 v160, v174
	v_mov_b32_e32 v161, v175
	v_pk_mul_f32 v[138:139], v[134:135], s[10:11] op_sel_hi:[1,0]
	v_pk_mul_f32 v[136:137], v[132:133], s[10:11] op_sel_hi:[1,0]
	v_pk_mul_f32 v[134:135], v[130:131], s[10:11] op_sel_hi:[1,0]
	v_pk_mul_f32 v[132:133], v[128:129], s[10:11] op_sel_hi:[1,0]
	v_lshlrev_b32_e32 v128, 16, v158
	v_and_b32_e32 v129, 0xffff0000, v158
	v_lshlrev_b32_e32 v130, 16, v159
	v_and_b32_e32 v131, 0xffff0000, v159
	v_lshlrev_b32_e32 v158, 16, v160
	v_and_b32_e32 v159, 0xffff0000, v160
	v_lshlrev_b32_e32 v160, 16, v161
	v_and_b32_e32 v161, 0xffff0000, v161
	v_pk_fma_f32 v[126:127], v[126:127], v[138:139], v[130:131]
	v_pk_fma_f32 v[124:125], v[124:125], v[136:137], v[128:129]
	v_pk_fma_f32 v[122:123], v[122:123], v[134:135], v[160:161]
	v_pk_fma_f32 v[120:121], v[120:121], v[132:133], v[158:159]
	v_cvt_pk_bf16_f32 v128, v124, v125
	v_cvt_pk_bf16_f32 v129, v126, v127
	v_pk_mul_f32 v[124:125], v[164:165], s[10:11] op_sel_hi:[1,0]
	v_cvt_pk_bf16_f32 v130, v120, v121
	v_cvt_pk_bf16_f32 v131, v122, v123
	v_mov_b32_e32 v158, v176
	v_mov_b32_e32 v159, v177
	v_mov_b32_e32 v160, v178
	v_mov_b32_e32 v161, v179
	v_or_b32_e32 v120, 16, v142
	v_ashrrev_i32_e32 v121, 31, v120
	v_lshlrev_b64 v[120:121], 11, v[120:121]
	v_lshl_add_u64 v[120:121], s[6:7], 0, v[120:121]
	v_lshl_add_u64 v[170:171], v[120:121], 0, v[144:145]
	v_pk_mul_f32 v[120:121], v[168:169], s[10:11] op_sel_hi:[1,0]
	v_pk_mul_f32 v[122:123], v[166:167], s[10:11] op_sel_hi:[1,0]
	v_pk_mul_f32 v[126:127], v[162:163], s[10:11] op_sel_hi:[1,0]
	global_store_dwordx4 v[140:141], v[128:131], off
	s_nop 0
	s_nop 0
	v_lshlrev_b32_e32 v128, 16, v158
	v_and_b32_e32 v129, 0xffff0000, v158
	v_lshlrev_b32_e32 v130, 16, v159
	v_and_b32_e32 v131, 0xffff0000, v159
	v_lshlrev_b32_e32 v158, 16, v160
	v_and_b32_e32 v159, 0xffff0000, v160
	v_lshlrev_b32_e32 v160, 16, v161
	v_and_b32_e32 v161, 0xffff0000, v161
	v_pk_fma_f32 v[114:115], v[114:115], v[120:121], v[130:131]
	v_pk_fma_f32 v[112:113], v[112:113], v[122:123], v[128:129]
	v_pk_fma_f32 v[128:129], v[110:111], v[124:125], v[160:161]
	v_pk_fma_f32 v[110:111], v[108:109], v[126:127], v[158:159]
	v_cvt_pk_bf16_f32 v108, v112, v113
	v_cvt_pk_bf16_f32 v109, v114, v115
	s_nop 0
	v_cvt_pk_bf16_f32 v110, v110, v111
	v_cvt_pk_bf16_f32 v111, v128, v129
	v_mov_b32_e32 v112, v180
	v_mov_b32_e32 v113, v181
	v_mov_b32_e32 v114, v182
	v_mov_b32_e32 v115, v183
	s_nop 0
	global_store_dwordx4 v[140:141], v[108:111], off offset:256
	s_nop 0
	s_nop 0
	v_lshlrev_b32_e32 v108, 16, v112
	v_and_b32_e32 v109, 0xffff0000, v112
	v_lshlrev_b32_e32 v110, 16, v113
	v_and_b32_e32 v111, 0xffff0000, v113
	v_lshlrev_b32_e32 v112, 16, v114
	v_and_b32_e32 v113, 0xffff0000, v114
	v_lshlrev_b32_e32 v114, 16, v115
	v_and_b32_e32 v115, 0xffff0000, v115
	v_pk_fma_f32 v[110:111], v[118:119], v[138:139], v[110:111]
	v_pk_fma_f32 v[108:109], v[116:117], v[136:137], v[108:109]
	v_pk_fma_f32 v[114:115], v[106:107], v[134:135], v[114:115]
	v_pk_fma_f32 v[106:107], v[104:105], v[132:133], v[112:113]
	v_cvt_pk_bf16_f32 v104, v108, v109
	v_cvt_pk_bf16_f32 v105, v110, v111
	v_or_b32_e32 v112, 32, v142
	v_cvt_pk_bf16_f32 v106, v106, v107
	v_cvt_pk_bf16_f32 v107, v114, v115
	v_mov_b32_e32 v108, v184
	v_mov_b32_e32 v109, v185
	v_mov_b32_e32 v110, v186
	v_mov_b32_e32 v111, v187
; __device__ __forceinline__ unsigned cvt_pk_bf16(float lo, float hi) { unsigned r; asm volatile("v_cvt_pk_bf16_f32 %0, %1, %2" : "=v"(r) : "v"(lo), "v"(hi)); return r; }
;     __device__ __forceinline__ void operator()(const f32x4 (&acc)[2][2][4][2], const Unit& u, int wr, int wc, int fr, int fq) const {
;     ...
;         for (int ai = 0; ai < 2; ++ai)
; #pragma unroll
;             for (int m = 0; m < 4; ++m) { const size_t ro = (size_t)(row0 + ai * HALF + m * 16) * DM + col0;
; #pragma unroll
;                 for (int bj = 0; bj < 2; ++bj) {
;                     f32x4 b0, b1;
;                     if (x0) { b0 = *(const f32x4*)(x0 + ro + bj * HALF); b1 = *(const f32x4*)(x0 + ro + bj * HALF + 4); }
;                     else { const u32x4 w = *(const u32x4*)(xb + ro + bj * HALF); b0 = (f32x4){bf_lo(w.x), bf_hi(w.x), bf_lo(w.y), bf_hi(w.y)}; b1 = (f32x4){bf_lo(w.z), bf_hi(w.z), bf_lo(w.w), bf_hi(w.w)}; }
;                     const f32x4 v0 = b0 + gv[bj][0] * acc[ai][bj][m][0], v1 = b1 + gv[bj][1] * acc[ai][bj][m][1];
;                     u32x4 o; o.x = cvt_pk_bf16(v0[0], v0[1]); o.y = cvt_pk_bf16(v0[2], v0[3]); o.z = cvt_pk_bf16(v1[0], v1[1]); o.w = cvt_pk_bf16(v1[2], v1[3]);
;                     *(u32x4*)(xout + ro + bj * HALF) = o; } }
	v_ashrrev_i32_e32 v113, 31, v112
	v_lshlrev_b64 v[112:113], 11, v[112:113]
	v_lshl_add_u64 v[112:113], s[6:7], 0, v[112:113]
	global_store_dwordx4 v[170:171], v[104:107], off
	s_nop 0
	v_lshl_add_u64 v[112:113], v[112:113], 0, v[144:145]
	v_lshlrev_b32_e32 v104, 16, v108
	v_and_b32_e32 v105, 0xffff0000, v108
	v_lshlrev_b32_e32 v106, 16, v109
	v_and_b32_e32 v107, 0xffff0000, v109
	v_lshlrev_b32_e32 v108, 16, v110
	v_and_b32_e32 v109, 0xffff0000, v110
	v_lshlrev_b32_e32 v110, 16, v111
	v_and_b32_e32 v111, 0xffff0000, v111
	v_pk_fma_f32 v[98:99], v[98:99], v[120:121], v[106:107]
	v_pk_fma_f32 v[96:97], v[96:97], v[122:123], v[104:105]
	v_pk_fma_f32 v[104:105], v[94:95], v[124:125], v[110:111]
	v_pk_fma_f32 v[94:95], v[92:93], v[126:127], v[108:109]
	v_cvt_pk_bf16_f32 v92, v96, v97
	v_cvt_pk_bf16_f32 v93, v98, v99
	s_nop 0
	v_cvt_pk_bf16_f32 v94, v94, v95
	v_cvt_pk_bf16_f32 v95, v104, v105
	v_mov_b32_e32 v96, v188
	v_mov_b32_e32 v97, v189
	v_mov_b32_e32 v98, v190
	v_mov_b32_e32 v99, v191
	s_nop 0
	global_store_dwordx4 v[170:171], v[92:95], off offset:256
	s_nop 0
	s_nop 0
	v_lshlrev_b32_e32 v92, 16, v96
	v_and_b32_e32 v93, 0xffff0000, v96
	v_lshlrev_b32_e32 v94, 16, v97
	v_and_b32_e32 v95, 0xffff0000, v97
	v_lshlrev_b32_e32 v96, 16, v98
	v_and_b32_e32 v97, 0xffff0000, v98
	v_lshlrev_b32_e32 v98, 16, v99
	v_and_b32_e32 v99, 0xffff0000, v99
	v_pk_fma_f32 v[94:95], v[102:103], v[138:139], v[94:95]
	v_pk_fma_f32 v[92:93], v[100:101], v[136:137], v[92:93]
	v_pk_fma_f32 v[98:99], v[90:91], v[134:135], v[98:99]
	v_pk_fma_f32 v[90:91], v[88:89], v[132:133], v[96:97]
	v_cvt_pk_bf16_f32 v88, v92, v93
	v_cvt_pk_bf16_f32 v89, v94, v95
	v_or_b32_e32 v96, 48, v142
	v_cvt_pk_bf16_f32 v90, v90, v91
	v_cvt_pk_bf16_f32 v91, v98, v99
	v_mov_b32_e32 v92, v192
	v_mov_b32_e32 v93, v193
	v_mov_b32_e32 v94, v194
	v_mov_b32_e32 v95, v195
	v_ashrrev_i32_e32 v97, 31, v96
	v_lshlrev_b64 v[96:97], 11, v[96:97]
	v_lshl_add_u64 v[96:97], s[6:7], 0, v[96:97]
	global_store_dwordx4 v[112:113], v[88:91], off
	s_nop 0
	v_lshl_add_u64 v[96:97], v[96:97], 0, v[144:145]
	v_lshlrev_b32_e32 v88, 16, v92
	v_and_b32_e32 v89, 0xffff0000, v92
	v_lshlrev_b32_e32 v90, 16, v93
	v_and_b32_e32 v91, 0xffff0000, v93
	v_lshlrev_b32_e32 v92, 16, v94
	v_and_b32_e32 v93, 0xffff0000, v94
	v_lshlrev_b32_e32 v94, 16, v95
	v_and_b32_e32 v95, 0xffff0000, v95
	v_pk_fma_f32 v[82:83], v[82:83], v[120:121], v[90:91]
	v_pk_fma_f32 v[80:81], v[80:81], v[122:123], v[88:89]
	v_pk_fma_f32 v[88:89], v[78:79], v[124:125], v[94:95]
	v_pk_fma_f32 v[78:79], v[76:77], v[126:127], v[92:93]
	v_cvt_pk_bf16_f32 v76, v80, v81
	v_cvt_pk_bf16_f32 v77, v82, v83
	s_nop 0
	v_cvt_pk_bf16_f32 v78, v78, v79
	v_cvt_pk_bf16_f32 v79, v88, v89
	v_mov_b32_e32 v80, v196
	v_mov_b32_e32 v81, v197
	v_mov_b32_e32 v82, v198
	v_mov_b32_e32 v83, v199
	s_nop 0
	global_store_dwordx4 v[112:113], v[76:79], off offset:256
	s_nop 0
	s_nop 0
	v_lshlrev_b32_e32 v76, 16, v80
	v_and_b32_e32 v77, 0xffff0000, v80
	v_lshlrev_b32_e32 v78, 16, v81
	v_and_b32_e32 v79, 0xffff0000, v81
	v_lshlrev_b32_e32 v80, 16, v82
	v_and_b32_e32 v81, 0xffff0000, v82
	v_lshlrev_b32_e32 v82, 16, v83
	v_and_b32_e32 v83, 0xffff0000, v83
	v_pk_fma_f32 v[78:79], v[86:87], v[138:139], v[78:79]
	v_pk_fma_f32 v[76:77], v[84:85], v[136:137], v[76:77]
	v_pk_fma_f32 v[82:83], v[74:75], v[134:135], v[82:83]
	v_pk_fma_f32 v[74:75], v[72:73], v[132:133], v[80:81]
	v_cvt_pk_bf16_f32 v72, v76, v77
	v_cvt_pk_bf16_f32 v73, v78, v79
	v_add_co_u32_e32 v80, vcc, s75, v140
	v_cvt_pk_bf16_f32 v74, v74, v75
	v_cvt_pk_bf16_f32 v75, v82, v83
	v_mov_b32_e32 v76, v200
	v_mov_b32_e32 v77, v201
	v_mov_b32_e32 v78, v202
	v_mov_b32_e32 v79, v203
	s_nop 0
	v_addc_co_u32_e32 v81, vcc, 0, v141, vcc
	global_store_dwordx4 v[96:97], v[72:75], off
	s_nop 0
	s_nop 0
	v_lshlrev_b32_e32 v72, 16, v76
	v_and_b32_e32 v73, 0xffff0000, v76
	v_lshlrev_b32_e32 v74, 16, v77
	v_and_b32_e32 v75, 0xffff0000, v77
	v_lshlrev_b32_e32 v76, 16, v78
	v_and_b32_e32 v77, 0xffff0000, v78
	v_lshlrev_b32_e32 v78, 16, v79
	v_and_b32_e32 v79, 0xffff0000, v79
	v_pk_fma_f32 v[70:71], v[70:71], v[120:121], v[74:75]
	v_pk_fma_f32 v[68:69], v[68:69], v[122:123], v[72:73]
	v_pk_fma_f32 v[72:73], v[66:67], v[124:125], v[78:79]
	v_pk_fma_f32 v[66:67], v[64:65], v[126:127], v[76:77]
	v_cvt_pk_bf16_f32 v64, v68, v69
	v_cvt_pk_bf16_f32 v65, v70, v71
	s_nop 0
	v_cvt_pk_bf16_f32 v66, v66, v67
	v_cvt_pk_bf16_f32 v67, v72, v73
	v_mov_b32_e32 v68, v204
	v_mov_b32_e32 v69, v205
	v_mov_b32_e32 v70, v206
	v_mov_b32_e32 v71, v207
	v_lshl_add_u64 v[72:73], v[140:141], 0, s[12:13]
	global_store_dwordx4 v[96:97], v[64:67], off offset:256
	s_nop 0
	s_nop 0
	v_lshlrev_b32_e32 v64, 16, v68
	v_and_b32_e32 v65, 0xffff0000, v68
	v_lshlrev_b32_e32 v66, 16, v69
	v_and_b32_e32 v67, 0xffff0000, v69
	v_lshlrev_b32_e32 v68, 16, v70
	v_and_b32_e32 v69, 0xffff0000, v70
	v_lshlrev_b32_e32 v70, 16, v71
	v_and_b32_e32 v71, 0xffff0000, v71
	v_pk_fma_f32 v[62:63], v[62:63], v[138:139], v[66:67]
	v_pk_fma_f32 v[60:61], v[60:61], v[136:137], v[64:65]
	v_pk_fma_f32 v[64:65], v[58:59], v[134:135], v[70:71]
	v_pk_fma_f32 v[58:59], v[56:57], v[132:133], v[68:69]
	v_cvt_pk_bf16_f32 v56, v60, v61
	v_cvt_pk_bf16_f32 v57, v62, v63
	s_nop 0
	v_cvt_pk_bf16_f32 v58, v58, v59
	v_cvt_pk_bf16_f32 v59, v64, v65
	v_mov_b32_e32 v60, v208
	v_mov_b32_e32 v61, v209
	v_mov_b32_e32 v62, v210
	v_mov_b32_e32 v63, v211
	v_add_co_u32_e32 v64, vcc, s76, v140
	global_store_dwordx4 v[80:81], v[56:59], off
	s_nop 0
	v_addc_co_u32_e32 v65, vcc, 0, v141, vcc
	v_lshlrev_b32_e32 v56, 16, v60
	v_and_b32_e32 v57, 0xffff0000, v60
	v_lshlrev_b32_e32 v58, 16, v61
	v_and_b32_e32 v59, 0xffff0000, v61
	v_lshlrev_b32_e32 v60, 16, v62
; __device__ __forceinline__ unsigned cvt_pk_bf16(float lo, float hi) { unsigned r; asm volatile("v_cvt_pk_bf16_f32 %0, %1, %2" : "=v"(r) : "v"(lo), "v"(hi)); return r; }
;     __device__ __forceinline__ void operator()(const f32x4 (&acc)[2][2][4][2], const Unit& u, int wr, int wc, int fr, int fq) const {
;     ...
;         for (int ai = 0; ai < 2; ++ai)
; #pragma unroll
;             for (int m = 0; m < 4; ++m) { const size_t ro = (size_t)(row0 + ai * HALF + m * 16) * DM + col0;
; #pragma unroll
;                 for (int bj = 0; bj < 2; ++bj) {
;                     f32x4 b0, b1;
;                     if (x0) { b0 = *(const f32x4*)(x0 + ro + bj * HALF); b1 = *(const f32x4*)(x0 + ro + bj * HALF + 4); }
;                     else { const u32x4 w = *(const u32x4*)(xb + ro + bj * HALF); b0 = (f32x4){bf_lo(w.x), bf_hi(w.x), bf_lo(w.y), bf_hi(w.y)}; b1 = (f32x4){bf_lo(w.z), bf_hi(w.z), bf_lo(w.w), bf_hi(w.w)}; }
;                     const f32x4 v0 = b0 + gv[bj][0] * acc[ai][bj][m][0], v1 = b1 + gv[bj][1] * acc[ai][bj][m][1];
;                     u32x4 o; o.x = cvt_pk_bf16(v0[0], v0[1]); o.y = cvt_pk_bf16(v0[2], v0[3]); o.z = cvt_pk_bf16(v1[0], v1[1]); o.w = cvt_pk_bf16(v1[2], v1[3]);
;                     *(u32x4*)(xout + ro + bj * HALF) = o; } }
	v_and_b32_e32 v61, 0xffff0000, v62
	v_lshlrev_b32_e32 v62, 16, v63
	v_and_b32_e32 v63, 0xffff0000, v63
	v_pk_fma_f32 v[54:55], v[54:55], v[120:121], v[58:59]
	v_pk_fma_f32 v[52:53], v[52:53], v[122:123], v[56:57]
	v_pk_fma_f32 v[56:57], v[46:47], v[124:125], v[62:63]
	v_pk_fma_f32 v[46:47], v[44:45], v[126:127], v[60:61]
	v_cvt_pk_bf16_f32 v44, v52, v53
	v_cvt_pk_bf16_f32 v45, v54, v55
	s_nop 0
	v_cvt_pk_bf16_f32 v46, v46, v47
	v_cvt_pk_bf16_f32 v47, v56, v57
	v_mov_b32_e32 v52, v212
	v_mov_b32_e32 v53, v213
	v_mov_b32_e32 v54, v214
	v_mov_b32_e32 v55, v215
	v_lshl_add_u64 v[56:57], v[140:141], 0, s[14:15]
	global_store_dwordx4 v[72:73], v[44:47], off offset:256
	s_nop 0
	s_nop 0
	v_lshlrev_b32_e32 v44, 16, v52
	v_and_b32_e32 v45, 0xffff0000, v52
	v_lshlrev_b32_e32 v46, 16, v53
	v_and_b32_e32 v47, 0xffff0000, v53
	v_lshlrev_b32_e32 v52, 16, v54
	v_and_b32_e32 v53, 0xffff0000, v54
	v_lshlrev_b32_e32 v54, 16, v55
	v_and_b32_e32 v55, 0xffff0000, v55
	v_pk_fma_f32 v[46:47], v[50:51], v[138:139], v[46:47]
	v_pk_fma_f32 v[44:45], v[48:49], v[136:137], v[44:45]
	v_pk_fma_f32 v[48:49], v[42:43], v[134:135], v[54:55]
	v_pk_fma_f32 v[42:43], v[40:41], v[132:133], v[52:53]
	v_cvt_pk_bf16_f32 v40, v44, v45
	v_cvt_pk_bf16_f32 v41, v46, v47
	s_nop 0
	v_cvt_pk_bf16_f32 v42, v42, v43
	v_cvt_pk_bf16_f32 v43, v48, v49
	v_mov_b32_e32 v44, v216
	v_mov_b32_e32 v45, v217
	v_mov_b32_e32 v46, v218
	v_mov_b32_e32 v47, v219
	v_add_co_u32_e32 v48, vcc, s77, v140
	global_store_dwordx4 v[64:65], v[40:43], off
	s_nop 0
	v_addc_co_u32_e32 v49, vcc, 0, v141, vcc
	v_lshlrev_b32_e32 v40, 16, v44
	v_and_b32_e32 v41, 0xffff0000, v44
	v_lshlrev_b32_e32 v42, 16, v45
	v_and_b32_e32 v43, 0xffff0000, v45
	v_lshlrev_b32_e32 v44, 16, v46
	v_and_b32_e32 v45, 0xffff0000, v46
	v_lshlrev_b32_e32 v46, 16, v47
	v_and_b32_e32 v47, 0xffff0000, v47
	v_pk_fma_f32 v[38:39], v[38:39], v[120:121], v[42:43]
	v_pk_fma_f32 v[36:37], v[36:37], v[122:123], v[40:41]
	v_pk_fma_f32 v[40:41], v[30:31], v[124:125], v[46:47]
	v_pk_fma_f32 v[30:31], v[28:29], v[126:127], v[44:45]
	v_cvt_pk_bf16_f32 v28, v36, v37
	v_cvt_pk_bf16_f32 v29, v38, v39
	s_nop 0
	v_cvt_pk_bf16_f32 v30, v30, v31
	v_cvt_pk_bf16_f32 v31, v40, v41
	v_mov_b32_e32 v36, v220
	v_mov_b32_e32 v37, v221
	v_mov_b32_e32 v38, v222
	v_mov_b32_e32 v39, v223
	v_lshl_add_u64 v[40:41], v[140:141], 0, s[16:17]
	global_store_dwordx4 v[56:57], v[28:31], off offset:256
	s_nop 0
	s_nop 0
	v_lshlrev_b32_e32 v28, 16, v36
	v_and_b32_e32 v29, 0xffff0000, v36
	v_lshlrev_b32_e32 v30, 16, v37
	v_and_b32_e32 v31, 0xffff0000, v37
	v_lshlrev_b32_e32 v36, 16, v38
	v_and_b32_e32 v37, 0xffff0000, v38
	v_lshlrev_b32_e32 v38, 16, v39
	v_and_b32_e32 v39, 0xffff0000, v39
	v_pk_fma_f32 v[30:31], v[34:35], v[138:139], v[30:31]
	v_pk_fma_f32 v[28:29], v[32:33], v[136:137], v[28:29]
	v_pk_fma_f32 v[32:33], v[26:27], v[134:135], v[38:39]
	v_pk_fma_f32 v[26:27], v[24:25], v[132:133], v[36:37]
	v_cvt_pk_bf16_f32 v24, v28, v29
	v_cvt_pk_bf16_f32 v25, v30, v31
	s_nop 0
	v_cvt_pk_bf16_f32 v26, v26, v27
	v_cvt_pk_bf16_f32 v27, v32, v33
	v_mov_b32_e32 v28, v224
	v_mov_b32_e32 v29, v225
	v_mov_b32_e32 v30, v226
	v_mov_b32_e32 v31, v227
	v_add_co_u32_e32 v32, vcc, s78, v140
	global_store_dwordx4 v[48:49], v[24:27], off
	s_nop 0
	v_addc_co_u32_e32 v33, vcc, 0, v141, vcc
	s_andn2_b64 vcc, exec, s[2:3]
	s_mov_b64 s[2:3], -1
	v_lshlrev_b32_e32 v24, 16, v28
	v_and_b32_e32 v25, 0xffff0000, v28
	v_lshlrev_b32_e32 v26, 16, v29
	v_and_b32_e32 v27, 0xffff0000, v29
	v_lshlrev_b32_e32 v28, 16, v30
	v_and_b32_e32 v29, 0xffff0000, v30
	v_lshlrev_b32_e32 v30, 16, v31
	v_and_b32_e32 v31, 0xffff0000, v31
	v_pk_fma_f32 v[22:23], v[22:23], v[120:121], v[26:27]
	v_pk_fma_f32 v[20:21], v[20:21], v[122:123], v[24:25]
	v_pk_fma_f32 v[24:25], v[14:15], v[124:125], v[30:31]
	v_pk_fma_f32 v[14:15], v[12:13], v[126:127], v[28:29]
	v_cvt_pk_bf16_f32 v12, v20, v21
	v_cvt_pk_bf16_f32 v13, v22, v23
	s_nop 0
	v_cvt_pk_bf16_f32 v14, v14, v15
	v_cvt_pk_bf16_f32 v15, v24, v25
	v_mov_b32_e32 v20, v228
	v_mov_b32_e32 v21, v229
	v_mov_b32_e32 v22, v230
	v_mov_b32_e32 v23, v231
	v_lshl_add_u64 v[24:25], v[140:141], 0, s[20:21]
	global_store_dwordx4 v[40:41], v[12:15], off offset:256
	s_nop 0
	s_nop 0
	v_lshlrev_b32_e32 v12, 16, v20
	v_and_b32_e32 v13, 0xffff0000, v20
	v_lshlrev_b32_e32 v14, 16, v21
	v_and_b32_e32 v15, 0xffff0000, v21
	v_lshlrev_b32_e32 v20, 16, v22
	v_and_b32_e32 v21, 0xffff0000, v22
	v_lshlrev_b32_e32 v22, 16, v23
	v_and_b32_e32 v23, 0xffff0000, v23
	v_pk_fma_f32 v[14:15], v[18:19], v[138:139], v[14:15]
	v_pk_fma_f32 v[12:13], v[16:17], v[136:137], v[12:13]
	v_pk_fma_f32 v[16:17], v[10:11], v[134:135], v[22:23]
	v_pk_fma_f32 v[10:11], v[8:9], v[132:133], v[20:21]
	v_cvt_pk_bf16_f32 v8, v12, v13
	v_cvt_pk_bf16_f32 v9, v14, v15
	s_nop 0
	v_cvt_pk_bf16_f32 v10, v10, v11
	v_cvt_pk_bf16_f32 v11, v16, v17
	v_mov_b32_e32 v12, v232
	v_mov_b32_e32 v13, v233
	v_mov_b32_e32 v14, v234
	v_mov_b32_e32 v15, v235
	s_nop 0
	global_store_dwordx4 v[32:33], v[8:11], off
	s_nop 0
	s_nop 0
	v_lshlrev_b32_e32 v8, 16, v12
	v_and_b32_e32 v9, 0xffff0000, v12
	v_lshlrev_b32_e32 v10, 16, v13
	v_and_b32_e32 v11, 0xffff0000, v13
	v_lshlrev_b32_e32 v12, 16, v14
	v_and_b32_e32 v13, 0xffff0000, v14
	v_lshlrev_b32_e32 v14, 16, v15
	v_and_b32_e32 v15, 0xffff0000, v15
	v_pk_fma_f32 v[4:5], v[4:5], v[122:123], v[8:9]
	v_pk_fma_f32 v[8:9], v[2:3], v[124:125], v[14:15]
	v_pk_fma_f32 v[2:3], v[0:1], v[126:127], v[12:13]
	v_pk_fma_f32 v[6:7], v[6:7], v[120:121], v[10:11]
	v_cvt_pk_bf16_f32 v0, v4, v5
	s_nop 0
	v_cvt_pk_bf16_f32 v1, v6, v7
	v_cvt_pk_bf16_f32 v2, v2, v3
	v_cvt_pk_bf16_f32 v3, v8, v9
	global_store_dwordx4 v[24:25], v[0:3], off offset:256
	s_cbranch_vccnz .LBB0_3276
	s_andn2_b64 vcc, exec, s[4:5]
	s_cbranch_vccnz .LBB0_3275
	s_barrier
	s_branch .LBB0_3275
